# static s_setprio 1 for waves 4-7 during the attention (P4,P16) and top-k (P9,P20) phases, on top of v062
# baseline (speedup 1.0000x reference)
.LBB0_333:
	s_cmp_lt_u32 s89, 4
	s_cbranch_scc1 .Laprio_4
	s_setprio 1

.LBB0_382:
	s_setprio 0
	s_cmp_gt_i32 s95, 5
	s_cselect_b64 s[4:5], -1, 0
	s_and_b64 s[0:1], s[20:21], s[4:5]
	s_andn2_b64 vcc, exec, s[0:1]
	s_cbranch_vccnz .LBB0_432
	s_waitcnt vmcnt(0)
	v_cmp_eq_u32_e32 vcc, 0, v0
	s_waitcnt vmcnt(0) lgkmcnt(0)
	s_barrier
	s_and_saveexec_b64 s[0:1], vcc
	s_cbranch_execz .LBB0_431
	v_mov_b32_e32 v1, s88
	s_waitcnt vmcnt(0) expcnt(0) lgkmcnt(0)
	ds_read_b32 v3, v1
	ds_read_b32 v1, v1 offset:4
	s_waitcnt lgkmcnt(1)
	v_cmp_ne_u32_e32 vcc, 0, v3
	s_cbranch_vccnz .LBB0_399
	v_readlane_b32 s6, v254, 0
	v_readlane_b32 s7, v254, 1
	s_load_dwordx2 s[10:11], s[6:7], 0x4
	s_add_u32 s6, s82, 0x4200
	s_addc_u32 s7, s83, 0
	s_add_u32 s8, s82, 0x4400
	s_addc_u32 s9, s83, 0
	s_waitcnt lgkmcnt(0)
	s_mul_i32 s2, s10, s92
	s_add_u32 s10, s82, 0x4500
	s_mul_i32 s2, s2, s11
	s_addc_u32 s11, s83, 0
	s_add_u32 s12, s82, 0x4600
	s_addc_u32 s13, s83, 0
	s_add_u32 s14, s82, 0x4700
	s_addc_u32 s15, s83, 0
	s_add_u32 s16, s82, 0x4800
	s_addc_u32 s17, s83, 0
	s_add_u32 s20, s82, 0x4900
	s_addc_u32 s21, s83, 0
	s_add_u32 s22, s82, 0x4a00
	s_addc_u32 s23, s83, 0
	s_add_u32 s26, s82, 0x4b00
	s_addc_u32 s27, s83, 0
	s_add_u32 s28, s82, 0x4c00
	s_addc_u32 s29, s83, 0
	s_add_u32 s30, s82, 0x4d00
	s_addc_u32 s31, s83, 0
	s_add_u32 s34, s82, 0x4e00
	s_addc_u32 s35, s83, 0
	s_add_u32 s36, s82, 0x4f00
	s_addc_u32 s37, s83, 0
	s_add_u32 s38, s82, 0x5000
	s_addc_u32 s39, s83, 0
	s_add_u32 s40, s82, 0x5100
	s_addc_u32 s41, s83, 0
	s_add_u32 s42, s82, 0x5200
	s_addc_u32 s43, s83, 0
	s_add_u32 s44, s82, 0x5300
	s_addc_u32 s45, s83, 0
	s_mov_b32 s33, 1
	v_mov_b32_e32 v17, 0
	s_branch .LBB0_387

.LBB0_688:
	s_setprio 0
	s_cmp_gt_i32 s95, 10
	s_cselect_b64 s[0:1], -1, 0
	s_and_b64 s[4:5], s[4:5], s[0:1]
	s_andn2_b64 vcc, exec, s[4:5]
	s_cbranch_vccnz .LBB0_738
	s_waitcnt vmcnt(0)
	v_cmp_eq_u32_e32 vcc, 0, v0
	s_waitcnt vmcnt(0) lgkmcnt(0)
	s_barrier
	s_and_saveexec_b64 s[4:5], vcc
	s_cbranch_execz .LBB0_737
	v_mov_b32_e32 v1, s88
	s_waitcnt vmcnt(0) expcnt(0) lgkmcnt(0)
	ds_read_b32 v3, v1
	ds_read_b32 v1, v1 offset:4
	s_waitcnt lgkmcnt(1)
	v_cmp_ne_u32_e32 vcc, 0, v3
	s_cbranch_vccnz .LBB0_705
	v_readlane_b32 s6, v254, 0
	v_readlane_b32 s7, v254, 1
	s_load_dwordx2 s[10:11], s[6:7], 0x4
	s_add_u32 s6, s82, 0x4200
	s_addc_u32 s7, s83, 0
	s_add_u32 s8, s82, 0x4400
	s_addc_u32 s9, s83, 0
	s_waitcnt lgkmcnt(0)
	s_mul_i32 s2, s10, s92
	s_add_u32 s10, s82, 0x4500
	s_mul_i32 s2, s2, s11
	s_addc_u32 s11, s83, 0
	s_add_u32 s12, s82, 0x4600
	s_addc_u32 s13, s83, 0
	s_add_u32 s14, s82, 0x4700
	s_addc_u32 s15, s83, 0
	s_add_u32 s16, s82, 0x4800
	s_addc_u32 s17, s83, 0
	s_add_u32 s18, s82, 0x4900
	s_addc_u32 s19, s83, 0
	s_add_u32 s20, s82, 0x4a00
	s_addc_u32 s21, s83, 0
	s_add_u32 s22, s82, 0x4b00
	s_addc_u32 s23, s83, 0
	s_add_u32 s26, s82, 0x4c00
	s_addc_u32 s27, s83, 0
	s_add_u32 s28, s82, 0x4d00
	s_addc_u32 s29, s83, 0
	s_add_u32 s30, s82, 0x4e00
	s_addc_u32 s31, s83, 0
	s_add_u32 s34, s82, 0x4f00
	s_addc_u32 s35, s83, 0
	s_add_u32 s36, s82, 0x5000
	s_addc_u32 s37, s83, 0
	s_add_u32 s38, s82, 0x5100
	s_addc_u32 s39, s83, 0
	s_add_u32 s40, s82, 0x5200
	s_addc_u32 s41, s83, 0
	s_add_u32 s42, s82, 0x5300
	s_addc_u32 s43, s83, 0
	s_mov_b32 s33, 1
	v_mov_b32_e32 v17, 0
	s_branch .LBB0_693

.LBB0_1163:
	s_setprio 0
	s_cmp_gt_i32 s95, 17
	v_readlane_b32 s2, v254, 44
	s_cselect_b64 s[0:1], -1, 0
	v_readlane_b32 s3, v254, 45
	s_and_b64 s[2:3], s[2:3], s[0:1]
	s_andn2_b64 vcc, exec, s[2:3]
	s_cbranch_vccnz .LBB0_1213
	s_waitcnt vmcnt(0)
	v_cmp_eq_u32_e32 vcc, 0, v0
	s_waitcnt vmcnt(0) lgkmcnt(0)
	s_barrier
	s_and_saveexec_b64 s[4:5], vcc
	s_cbranch_execz .LBB0_1212
	v_mov_b32_e32 v2, s88
	s_waitcnt vmcnt(0) expcnt(0) lgkmcnt(0)
	ds_read_b32 v4, v2
	ds_read_b32 v2, v2 offset:4
	s_waitcnt lgkmcnt(1)
	v_cmp_ne_u32_e32 vcc, 0, v4
	s_cbranch_vccnz .LBB0_1180
	v_readlane_b32 s6, v254, 0
	v_readlane_b32 s7, v254, 1
	s_load_dwordx2 s[2:3], s[6:7], 0x4
	s_add_u32 s6, s82, 0x4200
	s_addc_u32 s7, s83, 0
	s_add_u32 s8, s82, 0x4400
	s_addc_u32 s9, s83, 0
	v_readlane_b32 s10, v254, 42
	v_readlane_b32 s11, v254, 43
	s_waitcnt lgkmcnt(0)
	s_mul_i32 s2, s2, s10
	s_add_u32 s10, s82, 0x4500
	s_addc_u32 s11, s83, 0
	s_add_u32 s12, s82, 0x4600
	s_addc_u32 s13, s83, 0
	s_add_u32 s14, s82, 0x4700
	s_addc_u32 s15, s83, 0
	s_add_u32 s16, s82, 0x4800
	s_addc_u32 s17, s83, 0
	s_add_u32 s18, s82, 0x4900
	s_addc_u32 s19, s83, 0
	s_add_u32 s20, s82, 0x4a00
	s_addc_u32 s21, s83, 0
	s_add_u32 s22, s82, 0x4b00
	s_addc_u32 s23, s83, 0
	s_add_u32 s24, s82, 0x4c00
	s_addc_u32 s25, s83, 0
	s_add_u32 s26, s82, 0x4d00
	s_addc_u32 s27, s83, 0
	s_add_u32 s28, s82, 0x4e00
	s_addc_u32 s29, s83, 0
	s_add_u32 s30, s82, 0x4f00
	s_addc_u32 s31, s83, 0
	s_add_u32 s34, s82, 0x5000
	s_addc_u32 s35, s83, 0
	s_add_u32 s36, s82, 0x5100
	s_addc_u32 s37, s83, 0
	s_add_u32 s38, s82, 0x5200
	s_addc_u32 s39, s83, 0
	s_add_u32 s40, s82, 0x5300
	s_mul_i32 s2, s2, s3
	s_addc_u32 s41, s83, 0
	s_mov_b32 s3, 1
	v_mov_b32_e32 v18, 0
	s_branch .LBB0_1168

.LBB0_1437:
	s_setprio 0
	s_cmp_gt_i32 s95, 21
	s_cselect_b64 s[0:1], -1, 0
	s_and_b64 s[2:3], s[4:5], s[0:1]
	s_andn2_b64 vcc, exec, s[2:3]
	s_cbranch_vccnz .LBB0_1487
	s_waitcnt vmcnt(0)
	v_cmp_eq_u32_e32 vcc, 0, v0
	s_waitcnt vmcnt(0) lgkmcnt(0)
	s_barrier
	s_and_saveexec_b64 s[2:3], vcc
	s_cbranch_execz .LBB0_1486
	v_mov_b32_e32 v2, s88
	s_waitcnt vmcnt(0) expcnt(0) lgkmcnt(0)
	ds_read_b32 v4, v2
	ds_read_b32 v2, v2 offset:4
	s_waitcnt lgkmcnt(1)
	v_cmp_ne_u32_e32 vcc, 0, v4
	s_cbranch_vccnz .LBB0_1454
	v_readlane_b32 s4, v254, 0
	v_readlane_b32 s5, v254, 1
	s_load_dwordx2 s[8:9], s[4:5], 0x4
	s_add_u32 s4, s82, 0x4200
	s_addc_u32 s5, s83, 0
	s_add_u32 s6, s82, 0x4400
	s_addc_u32 s7, s83, 0
	v_readlane_b32 s10, v254, 42
	s_waitcnt lgkmcnt(0)
	s_mul_i32 s33, s8, s10
	s_add_u32 s8, s82, 0x4500
	s_mul_i32 s33, s33, s9
	s_addc_u32 s9, s83, 0
	v_readlane_b32 s11, v254, 43
	s_add_u32 s10, s82, 0x4600
	s_addc_u32 s11, s83, 0
	s_add_u32 s12, s82, 0x4700
	s_addc_u32 s13, s83, 0
	s_add_u32 s14, s82, 0x4800
	s_addc_u32 s15, s83, 0
	s_add_u32 s16, s82, 0x4900
	s_addc_u32 s17, s83, 0
	s_add_u32 s18, s82, 0x4a00
	s_addc_u32 s19, s83, 0
	s_add_u32 s20, s82, 0x4b00
	s_addc_u32 s21, s83, 0
	s_add_u32 s22, s82, 0x4c00
	s_addc_u32 s23, s83, 0
	s_add_u32 s24, s82, 0x4d00
	s_addc_u32 s25, s83, 0
	s_add_u32 s26, s82, 0x4e00
	s_addc_u32 s27, s83, 0
	s_add_u32 s28, s82, 0x4f00
	s_addc_u32 s29, s83, 0
	s_add_u32 s30, s82, 0x5000
	s_addc_u32 s31, s83, 0
	s_add_u32 s34, s82, 0x5100
	s_addc_u32 s35, s83, 0
	s_add_u32 s36, s82, 0x5200
	s_addc_u32 s37, s83, 0
	s_add_u32 s38, s82, 0x5300
	s_addc_u32 s39, s83, 0
	s_mov_b32 s46, 1
	v_mov_b32_e32 v18, 0
	s_branch .LBB0_1442
